# v24: v23 + attention tile loop with one workgroup barrier per half-step (DMA waits moved before the post-pv barrier, end-of-step barrier dropped)
# baseline (speedup 1.0000x reference)
; __device__ __forceinline__ void partialSM(f32x16& p0, f32x16& p1, float& m_reg, float& mn, float& alpha) {
;     float pmax = p0[0]; for (int r = 1; r < 16; ++r) pmax = fmaxf(pmax, p0[r]); for (int r = 0; r < 16; ++r) pmax = fmaxf(pmax, p1[r]);
;     { auto rr = __builtin_amdgcn_permlane32_swap(__float_as_uint(pmax), __float_as_uint(pmax), false, false);
;       pmax = fmaxf(__uint_as_float(rr[0]), __uint_as_float(rr[1])); }
;     constexpr float C2 = 1.4426950408889634f * SCALE;
;     if (__builtin_expect(__all((pmax - m_reg) * SCALE <= THR), 1)) { mn = m_reg; alpha = 1.f; }
;     else { mn = fmaxf(m_reg, pmax); alpha = __builtin_amdgcn_exp2f((m_reg - mn) * C2); m_reg = mn; }
;     const float mnL = -mn * C2;
;     for (int r = 0; r < 16; ++r) p0[r] = fmaf(p0[r], C2, mnL); for (int r = 0; r < 16; ++r) p1[r] = fmaf(p1[r], C2, mnL);
;     for (int r = 0; r < 16; ++r) p0[r] = __builtin_amdgcn_exp2f(p0[r]);
; template <class TIn, class TOut, int QS, int KS, int OS, bool BIAS, bool PREF = true>
; __device__ __forceinline__ void causal_swa_block(const BlockRef<TIn, TOut>& cur, const BlockRef<TIn, TOut>& nxt, int skv, int W, char* lds, Seam<TIn>& S) {
;     ...
;     for (int t = 1; t + 1 < NT; t += 2) {
;         HALF_STEP(pB0, pB1, mnB, alB, pA0, pA1, alA, t, 1, 0, 0);
;         HALF_STEP(pA0, pA1, mnA, alA, pB0, pB1, alB, t + 1, 0, 1, 1);
;     }
.LBB0_474:
	v_cndmask_b32_e64 v178, v162, v231, s[4:5]
	v_mul_f32_e32 v180, 0xbe0293ee, v178
	v_mov_b32_e32 v183, v180
	v_fmamk_f32 v162, v114, 0x3e0293ee, v180
	v_fmamk_f32 v163, v115, 0x3e0293ee, v180
	v_fmamk_f32 v164, v116, 0x3e0293ee, v180
	v_fmamk_f32 v165, v117, 0x3e0293ee, v180
	v_fmamk_f32 v166, v118, 0x3e0293ee, v180
	v_fmamk_f32 v167, v119, 0x3e0293ee, v180
	v_fmamk_f32 v168, v120, 0x3e0293ee, v180
	v_fmamk_f32 v169, v121, 0x3e0293ee, v180
	v_fmamk_f32 v181, v122, 0x3e0293ee, v180
	v_fmamk_f32 v182, v123, 0x3e0293ee, v180
	v_fmamk_f32 v124, v124, 0x3e0293ee, v180
	v_fmamk_f32 v125, v125, 0x3e0293ee, v180
	v_fmamk_f32 v126, v126, 0x3e0293ee, v180
	v_fmamk_f32 v127, v127, 0x3e0293ee, v180
	v_fmamk_f32 v128, v128, 0x3e0293ee, v180
	v_fmac_f32_e32 v183, 0x3e0293ee, v129
	v_exp_f32_e32 v175, v162
	v_exp_f32_e32 v177, v163
	v_exp_f32_e32 v173, v164
	v_exp_f32_e32 v176, v165
	v_exp_f32_e32 v172, v166
	v_exp_f32_e32 v174, v167
	v_exp_f32_e32 v170, v168
	v_exp_f32_e32 v171, v169
	v_exp_f32_e32 v165, v181
	v_exp_f32_e32 v168, v182
	v_exp_f32_e32 v163, v124
	v_exp_f32_e32 v166, v125
	v_exp_f32_e32 v162, v126
	v_exp_f32_e32 v169, v127
	v_exp_f32_e32 v164, v128
	v_exp_f32_e32 v167, v183
	s_addk_i32 s36, 0x80
	v_pk_fma_f32 v[128:129], v[98:99], s[18:19], v[180:181] op_sel_hi:[1,0,0]
	v_add_f32_e32 v98, v228, v229
	s_add_u32 s0, s0, 0x40000
	v_fmac_f32_e32 v98, v223, v224
	v_add_f32_e32 v224, v232, v233
	s_addc_u32 s1, s1, 0
	s_add_i32 s35, s35, 2
	v_pk_fma_f32 v[114:115], v[112:113], s[18:19], v[180:181] op_sel_hi:[1,0,0]
	v_pk_fma_f32 v[116:117], v[110:111], s[18:19], v[180:181] op_sel_hi:[1,0,0]
	v_pk_fma_f32 v[118:119], v[108:109], s[18:19], v[180:181] op_sel_hi:[1,0,0]
	v_pk_fma_f32 v[120:121], v[106:107], s[18:19], v[180:181] op_sel_hi:[1,0,0]
	v_pk_fma_f32 v[122:123], v[104:105], s[18:19], v[180:181] op_sel_hi:[1,0,0]
	v_pk_fma_f32 v[124:125], v[102:103], s[18:19], v[180:181] op_sel_hi:[1,0,0]
	v_pk_fma_f32 v[126:127], v[100:101], s[18:19], v[180:181] op_sel_hi:[1,0,0]
	v_fmac_f32_e32 v224, v98, v230
	v_add_u32_e32 v225, 0xffffff80, v225
	s_cmp_ge_i32 s35, s34
	v_add_u32_e32 v226, 0x200, v226
	v_mov_b32_e32 v223, v179
	s_waitcnt lgkmcnt(0)
	s_cbranch_scc1 .LBB0_493

; __device__ __forceinline__ void partialSM(f32x16& p0, f32x16& p1, float& m_reg, float& mn, float& alpha) {
;     float pmax = p0[0]; for (int r = 1; r < 16; ++r) pmax = fmaxf(pmax, p0[r]); for (int r = 0; r < 16; ++r) pmax = fmaxf(pmax, p1[r]);
;     { auto rr = __builtin_amdgcn_permlane32_swap(__float_as_uint(pmax), __float_as_uint(pmax), false, false);
;       pmax = fmaxf(__uint_as_float(rr[0]), __uint_as_float(rr[1])); }
;     constexpr float C2 = 1.4426950408889634f * SCALE;
;     if (__builtin_expect(__all((pmax - m_reg) * SCALE <= THR), 1)) { mn = m_reg; alpha = 1.f; }
;     else { mn = fmaxf(m_reg, pmax); alpha = __builtin_amdgcn_exp2f((m_reg - mn) * C2); m_reg = mn; }
;     const float mnL = -mn * C2;
;     for (int r = 0; r < 16; ++r) p0[r] = fmaf(p0[r], C2, mnL); for (int r = 0; r < 16; ++r) p1[r] = fmaf(p1[r], C2, mnL);
;     for (int r = 0; r < 16; ++r) p0[r] = __builtin_amdgcn_exp2f(p0[r]);
.LBB0_477:
	v_max_f32_e32 v66, v87, v87
	v_max_f32_e32 v67, v86, v86
	v_max_f32_e32 v66, v67, v66
	v_max3_f32 v66, v66, v88, v89
	v_max3_f32 v66, v66, v90, v91
	v_max3_f32 v66, v66, v92, v93
	v_max3_f32 v66, v66, v94, v95
	v_max3_f32 v66, v66, v96, v97
	v_max3_f32 v66, v66, v98, v99
	v_max3_f32 v66, v66, v100, v101
	v_max3_f32 v66, v66, v70, v71
	v_max3_f32 v66, v66, v72, v73
	v_max3_f32 v66, v66, v74, v75
	v_max3_f32 v66, v66, v76, v77
	v_max3_f32 v66, v66, v78, v79
	v_max3_f32 v66, v66, v80, v81
	v_max3_f32 v66, v66, v82, v83
	v_max3_f32 v66, v66, v84, v85
	v_mov_b32_e32 v67, v66
	s_nop 1
	v_permlane32_swap_b32_e32 v66, v67
	v_max_f32_e32 v67, v67, v67
	v_max_f32_e32 v66, v66, v66
	v_max_f32_e32 v66, v66, v67
	v_max_f32_e32 v68, v178, v178
	v_sub_f32_e32 v67, v66, v178
	v_max_f32_e32 v66, v68, v66
	v_sub_f32_e32 v68, v178, v66
	v_mul_f32_e32 v68, 0x3e0293ee, v68
	v_mul_f32_e32 v67, 0x3db504f3, v67
	v_exp_f32_e32 v68, v68
	v_cmp_ge_f32_e32 vcc, s38, v67
	s_cmp_eq_u64 vcc, exec
	s_cselect_b64 s[4:5], -1, 0
	s_waitcnt vmcnt(0)
	s_barrier
	v_cndmask_b32_e64 v230, v68, 1.0, s[4:5]
	v_cmp_gt_f32_e32 vcc, 1.0, v230
	s_add_u32 s98, s0, 0x9640000
	s_addc_u32 s99, s1, 0
	s_lshl_b32 s100, s75, 10
	s_add_i32 m0, s100, 0x0
	s_nop 0
	global_load_lds_dwordx4 v254, s[98:99]
	s_add_u32 s98, s98, 0x10000
	s_addc_u32 s99, s99, 0
	s_add_i32 m0, m0, 0x2000
	s_nop 0
	global_load_lds_dwordx4 v254, s[98:99]
	s_cbranch_vccz .LBB0_481
	s_and_saveexec_b64 s[20:21], s[2:3]
	ds_write_b32 v220, v230 offset:128
	s_or_b64 exec, exec, s[20:21]
	s_waitcnt lgkmcnt(0)
	ds_read_b128 v[102:105], v219 offset:224
	ds_read_b128 v[106:109], v219 offset:192
	ds_read_b128 v[110:113], v219 offset:160
	ds_read_b128 v[114:117], v219 offset:128
	s_waitcnt lgkmcnt(3)
	v_pk_mul_f32 v[64:65], v[64:65], v[104:105]
	s_waitcnt lgkmcnt(2)
	v_pk_mul_f32 v[60:61], v[60:61], v[108:109]
	s_waitcnt lgkmcnt(1)
	v_pk_mul_f32 v[56:57], v[56:57], v[112:113]
	s_waitcnt lgkmcnt(0)
	v_pk_mul_f32 v[52:53], v[52:53], v[116:117]
	v_pk_mul_f32 v[62:63], v[62:63], v[102:103]
	v_pk_mul_f32 v[58:59], v[58:59], v[106:107]
	v_pk_mul_f32 v[54:55], v[54:55], v[110:111]
	v_pk_mul_f32 v[50:51], v[50:51], v[114:115]
	v_pk_mul_f32 v[48:49], v[48:49], v[104:105]
	v_pk_mul_f32 v[44:45], v[44:45], v[108:109]
	v_pk_mul_f32 v[40:41], v[40:41], v[112:113]
	v_pk_mul_f32 v[36:37], v[36:37], v[116:117]
	v_pk_mul_f32 v[46:47], v[46:47], v[102:103]
	v_pk_mul_f32 v[42:43], v[42:43], v[106:107]
	v_pk_mul_f32 v[38:39], v[38:39], v[110:111]
	v_pk_mul_f32 v[34:35], v[34:35], v[114:115]
	v_pk_mul_f32 v[32:33], v[32:33], v[104:105]
	v_pk_mul_f32 v[28:29], v[28:29], v[108:109]
	v_pk_mul_f32 v[24:25], v[24:25], v[112:113]
	v_pk_mul_f32 v[20:21], v[20:21], v[116:117]
	v_pk_mul_f32 v[30:31], v[30:31], v[102:103]
	v_pk_mul_f32 v[26:27], v[26:27], v[106:107]
	v_pk_mul_f32 v[22:23], v[22:23], v[110:111]
	v_pk_mul_f32 v[18:19], v[18:19], v[114:115]
	v_pk_mul_f32 v[16:17], v[16:17], v[104:105]
	v_pk_mul_f32 v[12:13], v[12:13], v[108:109]
	v_pk_mul_f32 v[8:9], v[8:9], v[112:113]
	v_pk_mul_f32 v[4:5], v[4:5], v[116:117]
	v_pk_mul_f32 v[14:15], v[14:15], v[102:103]
	v_pk_mul_f32 v[10:11], v[10:11], v[106:107]
	v_pk_mul_f32 v[6:7], v[6:7], v[110:111]
	v_pk_mul_f32 v[2:3], v[2:3], v[114:115]
.LBB0_481:
	v_cndmask_b32_e64 v231, v66, v178, s[4:5]
	v_mul_f32_e32 v178, 0xbe0293ee, v231
	v_fmamk_f32 v66, v86, 0x3e0293ee, v178
	v_fmamk_f32 v67, v87, 0x3e0293ee, v178
	v_fmamk_f32 v68, v88, 0x3e0293ee, v178
	v_fmamk_f32 v69, v89, 0x3e0293ee, v178
	v_fmamk_f32 v102, v90, 0x3e0293ee, v178
	v_fmamk_f32 v103, v91, 0x3e0293ee, v178
	v_fmamk_f32 v104, v92, 0x3e0293ee, v178
	v_fmamk_f32 v105, v93, 0x3e0293ee, v178
	v_fmamk_f32 v106, v94, 0x3e0293ee, v178
	v_fmamk_f32 v107, v95, 0x3e0293ee, v178
	v_fmamk_f32 v108, v96, 0x3e0293ee, v178
	v_fmamk_f32 v109, v97, 0x3e0293ee, v178
	v_fmamk_f32 v98, v98, 0x3e0293ee, v178
	v_fmamk_f32 v99, v99, 0x3e0293ee, v178
	v_fmamk_f32 v100, v100, 0x3e0293ee, v178
	v_fmamk_f32 v101, v101, 0x3e0293ee, v178
	v_fmamk_f32 v86, v70, 0x3e0293ee, v178
	v_fmamk_f32 v95, v71, 0x3e0293ee, v178
	v_fmamk_f32 v96, v72, 0x3e0293ee, v178
	v_fmamk_f32 v97, v73, 0x3e0293ee, v178
	v_fmamk_f32 v179, v74, 0x3e0293ee, v178
	v_fmamk_f32 v87, v75, 0x3e0293ee, v178
	v_fmamk_f32 v88, v76, 0x3e0293ee, v178
	v_fmamk_f32 v89, v77, 0x3e0293ee, v178
	v_fmamk_f32 v90, v78, 0x3e0293ee, v178
	v_fmamk_f32 v91, v79, 0x3e0293ee, v178
	v_fmamk_f32 v92, v80, 0x3e0293ee, v178
	v_fmamk_f32 v93, v81, 0x3e0293ee, v178
	v_exp_f32_e32 v66, v66
	v_exp_f32_e32 v67, v67
	v_exp_f32_e32 v68, v68
	v_exp_f32_e32 v69, v69
	v_exp_f32_e32 v70, v102
	v_exp_f32_e32 v71, v103
	v_exp_f32_e32 v72, v104
	v_exp_f32_e32 v73, v105
	v_exp_f32_e32 v74, v106
	v_exp_f32_e32 v75, v107
	v_exp_f32_e32 v76, v108
	v_exp_f32_e32 v77, v109
	v_exp_f32_e32 v78, v98
	v_exp_f32_e32 v79, v99
	v_exp_f32_e32 v80, v100
	v_exp_f32_e32 v81, v101
	v_fmamk_f32 v94, v82, 0x3e0293ee, v178
	v_fmamk_f32 v180, v83, 0x3e0293ee, v178
	v_fmamk_f32 v181, v84, 0x3e0293ee, v178
	v_fmac_f32_e32 v178, 0x3e0293ee, v85
	s_waitcnt lgkmcnt(0)
	s_add_i32 s100, s35, 1
	s_cmp_lt_i32 s100, s34
	s_cbranch_scc0 .Lattn_k2skip_1
	s_add_u32 s98, s0, 0x7660000
	s_addc_u32 s99, s1, 0
	s_lshl_b32 s100, s75, 10
	s_add_i32 m0, s100, 0xc000
	s_nop 0
	global_load_lds_dwordx4 v253, s[98:99]
	s_add_u32 s98, s98, 0x10000
	s_addc_u32 s99, s99, 0
	s_add_i32 m0, m0, 0x2000
	s_nop 0
	global_load_lds_dwordx4 v253, s[98:99]

; __device__ __forceinline__ void partialSM(f32x16& p0, f32x16& p1, float& m_reg, float& mn, float& alpha) {
;     float pmax = p0[0]; for (int r = 1; r < 16; ++r) pmax = fmaxf(pmax, p0[r]); for (int r = 0; r < 16; ++r) pmax = fmaxf(pmax, p1[r]);
;     { auto rr = __builtin_amdgcn_permlane32_swap(__float_as_uint(pmax), __float_as_uint(pmax), false, false);
;       pmax = fmaxf(__uint_as_float(rr[0]), __uint_as_float(rr[1])); }
;     constexpr float C2 = 1.4426950408889634f * SCALE;
;     if (__builtin_expect(__all((pmax - m_reg) * SCALE <= THR), 1)) { mn = m_reg; alpha = 1.f; }
.LBB0_485:
	v_max_f32_e32 v178, v115, v115
	v_max_f32_e32 v179, v114, v114
	v_max_f32_e32 v178, v179, v178
	v_max3_f32 v178, v178, v116, v117
	v_max3_f32 v178, v178, v118, v119
	v_max3_f32 v178, v178, v120, v121
	v_max3_f32 v178, v178, v122, v123
	v_max3_f32 v178, v178, v124, v125
	v_max3_f32 v178, v178, v126, v127
	v_max3_f32 v178, v178, v128, v129
	v_max3_f32 v178, v178, v98, v99
	v_max3_f32 v178, v178, v100, v101
	v_max3_f32 v178, v178, v102, v103
	v_max3_f32 v178, v178, v104, v105
	v_max3_f32 v178, v178, v106, v107
	v_max3_f32 v178, v178, v108, v109
	v_max3_f32 v178, v178, v110, v111
	v_max3_f32 v178, v178, v112, v113
	v_mov_b32_e32 v179, v178
	s_nop 1
	v_permlane32_swap_b32_e32 v178, v179
	v_max_f32_e32 v179, v179, v179
	v_max_f32_e32 v178, v178, v178
	v_max_f32_e32 v178, v178, v179
	v_sub_f32_e32 v179, v178, v231
	v_mul_f32_e32 v179, 0x3db504f3, v179
	v_cmp_ge_f32_e32 vcc, s38, v179
	s_cmp_eq_u64 vcc, exec
	s_cselect_b64 s[4:5], -1, 0
	s_andn2_b64 vcc, exec, s[20:21]
	s_waitcnt vmcnt(0)
	s_barrier
	s_cbranch_vccnz .LBB0_487
	s_add_u32 s98, s0, 0x9660000
	s_addc_u32 s99, s1, 0
	s_lshl_b32 s100, s75, 10
	s_add_i32 m0, s100, 0x4000
	s_nop 0
	global_load_lds_dwordx4 v254, s[98:99]
	s_add_u32 s98, s98, 0x10000
	s_addc_u32 s99, s99, 0
	s_add_i32 m0, m0, 0x2000
	s_nop 0
	global_load_lds_dwordx4 v254, s[98:99]

; __device__ __forceinline__ void partialSM(f32x16& p0, f32x16& p1, float& m_reg, float& mn, float& alpha) {
;     float pmax = p0[0]; for (int r = 1; r < 16; ++r) pmax = fmaxf(pmax, p0[r]); for (int r = 0; r < 16; ++r) pmax = fmaxf(pmax, p1[r]);
;     { auto rr = __builtin_amdgcn_permlane32_swap(__float_as_uint(pmax), __float_as_uint(pmax), false, false);
;       pmax = fmaxf(__uint_as_float(rr[0]), __uint_as_float(rr[1])); }
;     constexpr float C2 = 1.4426950408889634f * SCALE;
;     if (__builtin_expect(__all((pmax - m_reg) * SCALE <= THR), 1)) { mn = m_reg; alpha = 1.f; }
;     else { mn = fmaxf(m_reg, pmax); alpha = __builtin_amdgcn_exp2f((m_reg - mn) * C2); m_reg = mn; }
;     const float mnL = -mn * C2;
;     for (int r = 0; r < 16; ++r) p0[r] = fmaf(p0[r], C2, mnL); for (int r = 0; r < 16; ++r) p1[r] = fmaf(p1[r], C2, mnL);
;     for (int r = 0; r < 16; ++r) p0[r] = __builtin_amdgcn_exp2f(p0[r]);
; template <class TIn, class TOut, int QS, int KS, int OS, bool BIAS, bool PREF = true>
; __device__ __forceinline__ void causal_swa_block(const BlockRef<TIn, TOut>& cur, const BlockRef<TIn, TOut>& nxt, int skv, int W, char* lds, Seam<TIn>& S) {
;     ...
;     for (int t = 1; t + 1 < NT; t += 2) {
;         HALF_STEP(pB0, pB1, mnB, alB, pA0, pA1, alA, t, 1, 0, 0);
;         HALF_STEP(pA0, pA1, mnA, alA, pB0, pB1, alB, t + 1, 0, 1, 1);
;     }
.LBB0_642:
	v_cndmask_b32_e64 v178, v162, v226, s[6:7]
	v_mul_f32_e32 v168, 0xbe0293ee, v178
	v_mov_b32_e32 v172, v168
	v_fmamk_f32 v114, v114, 0x3e0293ee, v168
	v_fmamk_f32 v115, v115, 0x3e0293ee, v168
	v_fmamk_f32 v116, v116, 0x3e0293ee, v168
	v_fmamk_f32 v117, v117, 0x3e0293ee, v168
	v_fmamk_f32 v118, v118, 0x3e0293ee, v168
	v_fmamk_f32 v119, v119, 0x3e0293ee, v168
	v_fmamk_f32 v120, v120, 0x3e0293ee, v168
	v_fmamk_f32 v121, v121, 0x3e0293ee, v168
	v_fmamk_f32 v122, v122, 0x3e0293ee, v168
	v_fmamk_f32 v123, v123, 0x3e0293ee, v168
	v_fmamk_f32 v167, v124, 0x3e0293ee, v168
	v_fmamk_f32 v125, v125, 0x3e0293ee, v168
	v_fmamk_f32 v169, v126, 0x3e0293ee, v168
	v_fmamk_f32 v170, v127, 0x3e0293ee, v168
	v_fmamk_f32 v171, v128, 0x3e0293ee, v168
	v_fmac_f32_e32 v172, 0x3e0293ee, v129
	v_exp_f32_e32 v163, v114
	v_exp_f32_e32 v165, v115
	v_exp_f32_e32 v129, v116
	v_exp_f32_e32 v164, v117
	v_exp_f32_e32 v128, v118
	v_exp_f32_e32 v162, v119
	v_exp_f32_e32 v126, v120
	v_exp_f32_e32 v127, v121
	v_exp_f32_e32 v121, v122
	v_exp_f32_e32 v124, v123
	v_exp_f32_e32 v119, v167
	v_exp_f32_e32 v122, v125
	v_exp_f32_e32 v118, v169
	v_exp_f32_e32 v125, v170
	v_exp_f32_e32 v120, v171
	v_exp_f32_e32 v123, v172
	s_addk_i32 s22, 0x80
	v_pk_fma_f32 v[116:117], v[98:99], s[16:17], v[168:169] op_sel_hi:[1,0,0]
	v_add_f32_e32 v98, v223, v224
	s_add_u32 s0, s0, 0x40000
	v_pk_fma_f32 v[112:113], v[112:113], s[16:17], v[168:169] op_sel_hi:[1,0,0]
	v_pk_fma_f32 v[110:111], v[110:111], s[16:17], v[168:169] op_sel_hi:[1,0,0]
	v_pk_fma_f32 v[108:109], v[108:109], s[16:17], v[168:169] op_sel_hi:[1,0,0]
	v_pk_fma_f32 v[106:107], v[106:107], s[16:17], v[168:169] op_sel_hi:[1,0,0]
	v_pk_fma_f32 v[104:105], v[104:105], s[16:17], v[168:169] op_sel_hi:[1,0,0]
	v_pk_fma_f32 v[102:103], v[102:103], s[16:17], v[168:169] op_sel_hi:[1,0,0]
	v_pk_fma_f32 v[114:115], v[100:101], s[16:17], v[168:169] op_sel_hi:[1,0,0]
	v_fmac_f32_e32 v98, v220, v216
	v_add_f32_e32 v216, v227, v228
	s_addc_u32 s1, s1, 0
	s_add_i32 s17, s17, 2
	v_fmac_f32_e32 v216, v98, v225
	v_add_u32_e32 v217, 0xffffff80, v217
	s_cmp_ge_i32 s17, s31
	v_add_u32_e32 v221, 0x200, v221
	v_mov_b32_e32 v220, v166
	s_waitcnt lgkmcnt(0)
	s_cbranch_scc1 .LBB0_659

; __device__ __forceinline__ void partialSM(f32x16& p0, f32x16& p1, float& m_reg, float& mn, float& alpha) {
;     float pmax = p0[0]; for (int r = 1; r < 16; ++r) pmax = fmaxf(pmax, p0[r]); for (int r = 0; r < 16; ++r) pmax = fmaxf(pmax, p1[r]);
;     { auto rr = __builtin_amdgcn_permlane32_swap(__float_as_uint(pmax), __float_as_uint(pmax), false, false);
;       pmax = fmaxf(__uint_as_float(rr[0]), __uint_as_float(rr[1])); }
;     constexpr float C2 = 1.4426950408889634f * SCALE;
;     if (__builtin_expect(__all((pmax - m_reg) * SCALE <= THR), 1)) { mn = m_reg; alpha = 1.f; }
;     else { mn = fmaxf(m_reg, pmax); alpha = __builtin_amdgcn_exp2f((m_reg - mn) * C2); m_reg = mn; }
;     const float mnL = -mn * C2;
;     for (int r = 0; r < 16; ++r) p0[r] = fmaf(p0[r], C2, mnL); for (int r = 0; r < 16; ++r) p1[r] = fmaf(p1[r], C2, mnL);
;     for (int r = 0; r < 16; ++r) p0[r] = __builtin_amdgcn_exp2f(p0[r]);
.LBB0_645:
	v_max_f32_e32 v66, v87, v87
	v_max_f32_e32 v67, v86, v86
	v_max_f32_e32 v66, v67, v66
	v_max3_f32 v66, v66, v88, v89
	v_max3_f32 v66, v66, v90, v91
	v_max3_f32 v66, v66, v92, v93
	v_max3_f32 v66, v66, v94, v95
	v_max3_f32 v66, v66, v96, v97
	v_max3_f32 v66, v66, v98, v99
	v_max3_f32 v66, v66, v100, v101
	v_max3_f32 v66, v66, v70, v71
	v_max3_f32 v66, v66, v72, v73
	v_max3_f32 v66, v66, v74, v75
	v_max3_f32 v66, v66, v76, v77
	v_max3_f32 v66, v66, v78, v79
	v_max3_f32 v66, v66, v80, v81
	v_max3_f32 v66, v66, v82, v83
	v_max3_f32 v66, v66, v84, v85
	v_mov_b32_e32 v67, v66
	s_nop 1
	v_permlane32_swap_b32_e32 v66, v67
	v_max_f32_e32 v67, v67, v67
	v_max_f32_e32 v66, v66, v66
	v_max_f32_e32 v66, v66, v67
	v_max_f32_e32 v68, v178, v178
	v_sub_f32_e32 v67, v66, v178
	v_max_f32_e32 v66, v68, v66
	v_sub_f32_e32 v68, v178, v66
	v_mul_f32_e32 v68, 0x3e0293ee, v68
	v_mul_f32_e32 v67, 0x3db504f3, v67
	v_exp_f32_e32 v68, v68
	v_cmp_ge_f32_e32 vcc, s26, v67
	s_cmp_eq_u64 vcc, exec
	s_cselect_b64 s[6:7], -1, 0
	s_waitcnt vmcnt(0)
	s_barrier
	v_cndmask_b32_e64 v225, v68, 1.0, s[6:7]
	v_cmp_gt_f32_e32 vcc, 1.0, v225
	s_add_u32 s98, s0, 0x9640000
	s_addc_u32 s99, s1, 0
	s_lshl_b32 s100, s75, 10
	s_add_i32 m0, s100, 0x0
	s_nop 0
	global_load_lds_dwordx4 v254, s[98:99]
	s_add_u32 s98, s98, 0x10000
	s_addc_u32 s99, s99, 0
	s_add_i32 m0, m0, 0x2000
	s_nop 0
	global_load_lds_dwordx4 v254, s[98:99]
	s_cbranch_vccz .LBB0_649
	s_and_saveexec_b64 s[18:19], s[4:5]
	ds_write_b32 v218, v225 offset:128
	s_or_b64 exec, exec, s[18:19]
	s_waitcnt lgkmcnt(0)
	ds_read_b128 v[102:105], v201 offset:224
	ds_read_b128 v[106:109], v201 offset:192
	ds_read_b128 v[110:113], v201 offset:160
	ds_read_b128 v[114:117], v201 offset:128
	s_waitcnt lgkmcnt(3)
	v_pk_mul_f32 v[64:65], v[64:65], v[104:105]
	s_waitcnt lgkmcnt(2)
	v_pk_mul_f32 v[60:61], v[60:61], v[108:109]
	s_waitcnt lgkmcnt(1)
	v_pk_mul_f32 v[56:57], v[56:57], v[112:113]
	s_waitcnt lgkmcnt(0)
	v_pk_mul_f32 v[52:53], v[52:53], v[116:117]
	v_pk_mul_f32 v[62:63], v[62:63], v[102:103]
	v_pk_mul_f32 v[58:59], v[58:59], v[106:107]
	v_pk_mul_f32 v[54:55], v[54:55], v[110:111]
	v_pk_mul_f32 v[50:51], v[50:51], v[114:115]
	v_pk_mul_f32 v[48:49], v[48:49], v[104:105]
	v_pk_mul_f32 v[44:45], v[44:45], v[108:109]
	v_pk_mul_f32 v[40:41], v[40:41], v[112:113]
	v_pk_mul_f32 v[36:37], v[36:37], v[116:117]
	v_pk_mul_f32 v[46:47], v[46:47], v[102:103]
	v_pk_mul_f32 v[42:43], v[42:43], v[106:107]
	v_pk_mul_f32 v[38:39], v[38:39], v[110:111]
	v_pk_mul_f32 v[34:35], v[34:35], v[114:115]
	v_pk_mul_f32 v[32:33], v[32:33], v[104:105]
	v_pk_mul_f32 v[28:29], v[28:29], v[108:109]
	v_pk_mul_f32 v[24:25], v[24:25], v[112:113]
	v_pk_mul_f32 v[20:21], v[20:21], v[116:117]
	v_pk_mul_f32 v[30:31], v[30:31], v[102:103]
	v_pk_mul_f32 v[26:27], v[26:27], v[106:107]
	v_pk_mul_f32 v[22:23], v[22:23], v[110:111]
	v_pk_mul_f32 v[18:19], v[18:19], v[114:115]
	v_pk_mul_f32 v[16:17], v[16:17], v[104:105]
	v_pk_mul_f32 v[12:13], v[12:13], v[108:109]
	v_pk_mul_f32 v[8:9], v[8:9], v[112:113]
	v_pk_mul_f32 v[4:5], v[4:5], v[116:117]
	v_pk_mul_f32 v[14:15], v[14:15], v[102:103]
	v_pk_mul_f32 v[10:11], v[10:11], v[106:107]
	v_pk_mul_f32 v[6:7], v[6:7], v[110:111]
	v_pk_mul_f32 v[2:3], v[2:3], v[114:115]
.LBB0_649:
	v_cndmask_b32_e64 v226, v66, v178, s[6:7]
	v_mul_f32_e32 v178, 0xbe0293ee, v226
	v_fmamk_f32 v66, v86, 0x3e0293ee, v178
	v_fmamk_f32 v67, v87, 0x3e0293ee, v178
	v_fmamk_f32 v68, v88, 0x3e0293ee, v178
	v_fmamk_f32 v69, v89, 0x3e0293ee, v178
	v_fmamk_f32 v102, v90, 0x3e0293ee, v178
	v_fmamk_f32 v103, v91, 0x3e0293ee, v178
	v_fmamk_f32 v104, v92, 0x3e0293ee, v178
	v_fmamk_f32 v105, v93, 0x3e0293ee, v178
	v_fmamk_f32 v106, v94, 0x3e0293ee, v178
	v_fmamk_f32 v107, v95, 0x3e0293ee, v178
	v_fmamk_f32 v108, v96, 0x3e0293ee, v178
	v_fmamk_f32 v109, v97, 0x3e0293ee, v178
	v_fmamk_f32 v98, v98, 0x3e0293ee, v178
	v_fmamk_f32 v99, v99, 0x3e0293ee, v178
	v_fmamk_f32 v100, v100, 0x3e0293ee, v178
	v_fmamk_f32 v101, v101, 0x3e0293ee, v178
	v_fmamk_f32 v86, v70, 0x3e0293ee, v178
	v_fmamk_f32 v95, v71, 0x3e0293ee, v178
	v_fmamk_f32 v96, v72, 0x3e0293ee, v178
	v_fmamk_f32 v97, v73, 0x3e0293ee, v178
	v_fmamk_f32 v179, v74, 0x3e0293ee, v178
	v_fmamk_f32 v87, v75, 0x3e0293ee, v178
	v_fmamk_f32 v88, v76, 0x3e0293ee, v178
	v_fmamk_f32 v89, v77, 0x3e0293ee, v178
	v_fmamk_f32 v90, v78, 0x3e0293ee, v178
	v_fmamk_f32 v91, v79, 0x3e0293ee, v178
	v_fmamk_f32 v92, v80, 0x3e0293ee, v178
	v_fmamk_f32 v93, v81, 0x3e0293ee, v178
	v_exp_f32_e32 v66, v66
	v_exp_f32_e32 v67, v67
	v_exp_f32_e32 v68, v68
	v_exp_f32_e32 v69, v69
	v_exp_f32_e32 v70, v102
	v_exp_f32_e32 v71, v103
	v_exp_f32_e32 v72, v104
	v_exp_f32_e32 v73, v105
	v_exp_f32_e32 v74, v106
	v_exp_f32_e32 v75, v107
	v_exp_f32_e32 v76, v108
	v_exp_f32_e32 v77, v109
	v_exp_f32_e32 v78, v98
	v_exp_f32_e32 v79, v99
	v_exp_f32_e32 v80, v100
	v_exp_f32_e32 v81, v101
	v_fmamk_f32 v94, v82, 0x3e0293ee, v178
	v_fmamk_f32 v180, v83, 0x3e0293ee, v178
	v_fmamk_f32 v181, v84, 0x3e0293ee, v178
	v_fmac_f32_e32 v178, 0x3e0293ee, v85
	s_waitcnt lgkmcnt(0)
	s_add_i32 s100, s17, 1
	s_cmp_lt_i32 s100, s31
	s_cbranch_scc0 .Lattn_k2skip_2
	s_add_u32 s98, s0, 0x7660000
	s_addc_u32 s99, s1, 0
	s_lshl_b32 s100, s75, 10
	s_add_i32 m0, s100, 0xc000
	s_nop 0
	global_load_lds_dwordx4 v253, s[98:99]
	s_add_u32 s98, s98, 0x10000
	s_addc_u32 s99, s99, 0
	s_add_i32 m0, m0, 0x2000
	s_nop 0
	global_load_lds_dwordx4 v253, s[98:99]

; __device__ __forceinline__ void partialSM(f32x16& p0, f32x16& p1, float& m_reg, float& mn, float& alpha) {
;     float pmax = p0[0]; for (int r = 1; r < 16; ++r) pmax = fmaxf(pmax, p0[r]); for (int r = 0; r < 16; ++r) pmax = fmaxf(pmax, p1[r]);
;     { auto rr = __builtin_amdgcn_permlane32_swap(__float_as_uint(pmax), __float_as_uint(pmax), false, false);
;       pmax = fmaxf(__uint_as_float(rr[0]), __uint_as_float(rr[1])); }
;     constexpr float C2 = 1.4426950408889634f * SCALE;
;     if (__builtin_expect(__all((pmax - m_reg) * SCALE <= THR), 1)) { mn = m_reg; alpha = 1.f; }
.LBB0_653:
	v_max_f32_e32 v178, v115, v115
	v_max_f32_e32 v179, v114, v114
	v_max_f32_e32 v178, v179, v178
	v_max3_f32 v178, v178, v116, v117
	v_max3_f32 v178, v178, v118, v119
	v_max3_f32 v178, v178, v120, v121
	v_max3_f32 v178, v178, v122, v123
	v_max3_f32 v178, v178, v124, v125
	v_max3_f32 v178, v178, v126, v127
	v_max3_f32 v178, v178, v128, v129
	v_max3_f32 v178, v178, v98, v99
	v_max3_f32 v178, v178, v100, v101
	v_max3_f32 v178, v178, v102, v103
	v_max3_f32 v178, v178, v104, v105
	v_max3_f32 v178, v178, v106, v107
	v_max3_f32 v178, v178, v108, v109
	v_max3_f32 v178, v178, v110, v111
	v_max3_f32 v178, v178, v112, v113
	v_mov_b32_e32 v179, v178
	s_nop 1
	v_permlane32_swap_b32_e32 v178, v179
	v_max_f32_e32 v179, v179, v179
	v_max_f32_e32 v178, v178, v178
	v_max_f32_e32 v178, v178, v179
	v_sub_f32_e32 v179, v178, v226
	v_mul_f32_e32 v179, 0x3db504f3, v179
	v_cmp_ge_f32_e32 vcc, s26, v179
	s_cmp_eq_u64 vcc, exec
	s_cselect_b64 s[6:7], -1, 0
	s_andn2_b64 vcc, exec, s[18:19]
	s_waitcnt vmcnt(0)
	s_barrier
	s_cbranch_vccnz .LBB0_655
	s_add_u32 s98, s0, 0x9660000
	s_addc_u32 s99, s1, 0
	s_lshl_b32 s100, s75, 10
	s_add_i32 m0, s100, 0x4000
	s_nop 0
	global_load_lds_dwordx4 v254, s[98:99]
	s_add_u32 s98, s98, 0x10000
	s_addc_u32 s99, s99, 0
	s_add_i32 m0, m0, 0x2000
	s_nop 0
	global_load_lds_dwordx4 v254, s[98:99]
